# opt1 + scanB compute loop: all LDS reads hoisted behind one wait (fresh VGPRs)
# baseline (speedup 1.0000x reference)
.LBB0_837:
	s_mul_hi_u32 s18, s16, 0xcccccccd
	s_lshr_b32 s18, s18, 2
	s_mul_i32 s18, s18, 0xfffe2000
	v_add_u32_e32 v96, s73, v53
	v_add3_u32 v210, v55, s18, v96
	v_add3_u32 v211, v60, s18, v96
	ds_read2st64_b64 v[110:113], v210 offset1:8
	ds_read2st64_b64 v[114:117], v211 offset0:16 offset1:20
	v_add3_u32 v212, v61, s18, v96
	ds_read2st64_b64 v[118:121], v212 offset0:16 offset1:20
	ds_read2st64_b64 v[122:125], v211 offset1:4
	ds_read2st64_b64 v[126:129], v212 offset1:4
	v_add3_u32 v213, v59, s18, v96
	v_add3_u32 v214, v54, s18, v96
	ds_read2st64_b64 v[130:133], v213 offset0:16 offset1:20
	ds_read2st64_b64 v[134:137], v214 offset0:64 offset1:68
	ds_read2st64_b64 v[138:141], v213 offset1:4
	ds_read2st64_b64 v[142:145], v214 offset0:48 offset1:52
	v_add3_u32 v215, v56, s18, v96
	ds_read2st64_b64 v[146:149], v215 offset1:8
	ds_read2st64_b64 v[150:153], v211 offset0:24 offset1:28
	v_add3_u32 v216, v57, s18, v96
	ds_read2st64_b64 v[154:157], v216 offset1:8
	ds_read2st64_b64 v[158:161], v212 offset0:24 offset1:28
	ds_read2st64_b64 v[162:165], v211 offset0:8 offset1:12
	ds_read2st64_b64 v[166:169], v212 offset0:8 offset1:12
	ds_read2st64_b64 v[170:173], v213 offset0:24 offset1:28
	ds_read2st64_b64 v[174:177], v214 offset0:72 offset1:76
	ds_read2st64_b64 v[178:181], v213 offset0:8 offset1:12
	ds_read2st64_b64 v[182:185], v214 offset0:56 offset1:60
	v_add3_u32 v217, v58, s18, v96
	ds_read2st64_b64 v[186:189], v217 offset0:80 offset1:88
	v_cvt_pk_bf16_f32 v20, v0, v1
	v_cvt_pk_bf16_f32 v21, v2, v3
	v_cvt_pk_bf16_f32 v18, v12, v13
	v_cvt_pk_bf16_f32 v19, v14, v15
	v_cvt_pk_bf16_f32 v22, v4, v5
	v_cvt_pk_bf16_f32 v23, v6, v7
	v_cvt_pk_bf16_f32 v16, v8, v9
	v_cvt_pk_bf16_f32 v17, v10, v11
	s_waitcnt lgkmcnt(0)
	v_lshlrev_b32_e32 v4, 16, v112
	v_and_b32_e32 v5, 0xffff0000, v112
	v_lshlrev_b32_e32 v6, 16, v113
	v_and_b32_e32 v7, 0xffff0000, v113
	v_lshlrev_b32_e32 v8, 16, v110
	v_and_b32_e32 v9, 0xffff0000, v110
	v_lshlrev_b32_e32 v10, 16, v111
	v_and_b32_e32 v11, 0xffff0000, v111
	v_mov_b32_e32 v0, v114
	v_mov_b32_e32 v1, v115
	v_mov_b32_e32 v2, v118
	v_mov_b32_e32 v3, v119
	s_nop 1
	v_mfma_f32_16x16x32_bf16 v[0:3], v[0:3], v[20:23], v[4:7]
	s_add_i32 s86, s86, s85
	s_nop 1
	s_ashr_i32 s87, s86, 31
	s_lshl_b64 s[86:87], s[86:87], 11
	v_mov_b32_e32 v92, v134
	v_mov_b32_e32 v90, v130
	v_mov_b32_e32 v91, v131
	v_mov_b32_e32 v93, v135
	v_mov_b32_e32 v74, v122
	v_mov_b32_e32 v75, v123
	v_mfma_f32_16x16x32_bf16 v[0:3], v[90:93], v[16:19], v[0:3]
	v_mov_b32_e32 v76, v126
	v_mov_b32_e32 v77, v127
	v_lshl_add_u64 v[94:95], v[32:33], 0, s[86:87]
	s_nop 4
	v_cvt_pk_bf16_f32 v0, v0, s0
	global_store_short v[94:95], v0, off
	v_cvt_pk_bf16_f32 v4, v1, s0
	v_lshl_add_u64 v[0:1], v[94:95], 0, s[70:71]
	global_store_short v[0:1], v4, off
	v_cvt_pk_bf16_f32 v2, v2, s0
	v_lshl_add_u64 v[0:1], v[0:1], 0, s[70:71]
	global_store_short v[0:1], v2, off
	v_mov_b32_e32 v98, v138
	v_mov_b32_e32 v99, v139
	v_mov_b32_e32 v100, v142
	v_mov_b32_e32 v101, v143
	v_mfma_f32_16x16x32_bf16 v[8:11], v[74:77], v[20:23], v[8:11]
	v_mov_b32_e32 v62, v116
	v_mov_b32_e32 v63, v117
	v_cvt_pk_bf16_f32 v2, v3, s0
	v_lshl_add_u64 v[12:13], v[0:1], 0, s[70:71]
	global_store_short v[12:13], v2, off
	v_mfma_f32_16x16x32_bf16 v[0:3], v[98:101], v[16:19], v[8:11]
	v_mov_b32_e32 v78, v132
	v_mov_b32_e32 v79, v133
	v_mov_b32_e32 v70, v124
	v_lshlrev_b32_e32 v8, 16, v148
	v_and_b32_e32 v9, 0xffff0000, v148
	v_lshlrev_b32_e32 v10, 16, v149
	v_and_b32_e32 v11, 0xffff0000, v149
	v_mov_b32_e32 v71, v125
	v_lshlrev_b32_e32 v90, 16, v146
	v_mov_b32_e32 v64, v120
	v_mov_b32_e32 v65, v121
	s_nop 1
	v_mfma_f32_16x16x32_bf16 v[4:7], v[62:65], v[20:23], v[8:11]
	v_and_b32_e32 v91, 0xffff0000, v146
	v_lshlrev_b32_e32 v92, 16, v147
	v_and_b32_e32 v93, 0xffff0000, v147
	v_mov_b32_e32 v80, v136
	v_mov_b32_e32 v81, v137
	s_nop 1
	v_mfma_f32_16x16x32_bf16 v[4:7], v[78:81], v[16:19], v[4:7]
	v_lshl_add_u64 v[8:9], v[12:13], 0, s[68:69]
	v_mov_b32_e32 v86, v140
	v_mov_b32_e32 v87, v141
	v_mov_b32_e32 v78, v150
	s_nop 3
	v_cvt_pk_bf16_f32 v4, v4, s0
	global_store_short v[8:9], v4, off
	v_cvt_pk_bf16_f32 v10, v5, s0
	v_lshl_add_u64 v[4:5], v[8:9], 0, s[70:71]
	global_store_short v[4:5], v10, off
	v_cvt_pk_bf16_f32 v6, v6, s0
	v_lshl_add_u64 v[4:5], v[4:5], 0, s[70:71]
	global_store_short v[4:5], v6, off
	v_mov_b32_e32 v72, v128
	v_mov_b32_e32 v73, v129
	s_nop 1
	v_mfma_f32_16x16x32_bf16 v[8:11], v[70:73], v[20:23], v[90:93]
	v_cvt_pk_bf16_f32 v6, v7, s0
	v_lshl_add_u64 v[94:95], v[4:5], 0, s[70:71]
	global_store_short v[94:95], v6, off
	v_mov_b32_e32 v88, v144
	v_mov_b32_e32 v89, v145
	s_nop 1
	v_mfma_f32_16x16x32_bf16 v[4:7], v[86:89], v[16:19], v[8:11]
	v_lshlrev_b32_e32 v62, 16, v154
	v_and_b32_e32 v63, 0xffff0000, v154
	v_lshlrev_b32_e32 v64, 16, v155
	v_lshlrev_b32_e32 v8, 16, v156
	v_and_b32_e32 v9, 0xffff0000, v156
	v_lshlrev_b32_e32 v10, 16, v157
	v_and_b32_e32 v11, 0xffff0000, v157
	v_and_b32_e32 v65, 0xffff0000, v155
	v_mov_b32_e32 v79, v151
	v_mov_b32_e32 v80, v158
	v_mov_b32_e32 v81, v159
	v_mov_b32_e32 v82, v162
	v_mov_b32_e32 v83, v163
	v_mfma_f32_16x16x32_bf16 v[8:11], v[78:81], v[20:23], v[8:11]
	v_mov_b32_e32 v102, v170
	v_mov_b32_e32 v103, v171
	v_mov_b32_e32 v104, v174
	v_mov_b32_e32 v105, v175
	v_mov_b32_e32 v84, v166
	v_mov_b32_e32 v85, v167
	v_mfma_f32_16x16x32_bf16 v[8:11], v[102:105], v[16:19], v[8:11]
	v_lshl_add_u64 v[12:13], v[94:95], 0, s[68:69]
	v_mov_b32_e32 v106, v178
	v_mov_b32_e32 v107, v179
	s_nop 4
	v_cvt_pk_bf16_f32 v8, v8, s0
	global_store_short v[12:13], v8, off
	v_cvt_pk_bf16_f32 v66, v9, s0
	v_lshl_add_u64 v[8:9], v[12:13], 0, s[70:71]
	global_store_short v[8:9], v66, off
	v_cvt_pk_bf16_f32 v10, v10, s0
	v_lshl_add_u64 v[8:9], v[8:9], 0, s[70:71]
	global_store_short v[8:9], v10, off
	v_mov_b32_e32 v108, v182
	v_mov_b32_e32 v109, v183
	v_mfma_f32_16x16x32_bf16 v[62:65], v[82:85], v[20:23], v[62:65]
	v_mov_b32_e32 v12, v152
	v_mov_b32_e32 v13, v153
	v_cvt_pk_bf16_f32 v10, v11, s0
	v_lshl_add_u64 v[66:67], v[8:9], 0, s[70:71]
	global_store_short v[66:67], v10, off
	v_mfma_f32_16x16x32_bf16 v[8:11], v[106:109], v[16:19], v[62:65]
	v_mov_b32_e32 v78, v172
	v_mov_b32_e32 v79, v173
	v_mov_b32_e32 v74, v164
	v_lshlrev_b32_e32 v62, 16, v188
	v_and_b32_e32 v63, 0xffff0000, v188
	v_lshlrev_b32_e32 v64, 16, v189
	v_and_b32_e32 v65, 0xffff0000, v189
	v_mov_b32_e32 v75, v165
	v_lshlrev_b32_e32 v84, 16, v186
	v_mov_b32_e32 v14, v160
	v_mov_b32_e32 v15, v161
	s_nop 1
	v_mfma_f32_16x16x32_bf16 v[12:15], v[12:15], v[20:23], v[62:65]
	v_and_b32_e32 v85, 0xffff0000, v186
	v_lshlrev_b32_e32 v86, 16, v187
	v_and_b32_e32 v87, 0xffff0000, v187
	v_mov_b32_e32 v80, v176
	v_mov_b32_e32 v81, v177
	s_nop 1
	v_mfma_f32_16x16x32_bf16 v[12:15], v[78:81], v[16:19], v[12:15]
	v_mov_b32_e32 v98, v180
	v_mov_b32_e32 v99, v181
	v_lshl_add_u64 v[62:63], v[66:67], 0, s[68:69]
	v_mov_b32_e32 v76, v168
	v_mov_b32_e32 v77, v169
	s_nop 1
	v_mfma_f32_16x16x32_bf16 v[20:23], v[74:77], v[20:23], v[84:87]
	s_nop 3
	v_cvt_pk_bf16_f32 v12, v12, s0
	global_store_short v[62:63], v12, off
	v_cvt_pk_bf16_f32 v64, v13, s0
	v_lshl_add_u64 v[12:13], v[62:63], 0, s[70:71]
	global_store_short v[12:13], v64, off
	v_cvt_pk_bf16_f32 v14, v14, s0
	v_lshl_add_u64 v[12:13], v[12:13], 0, s[70:71]
	global_store_short v[12:13], v14, off
	v_cvt_pk_bf16_f32 v14, v15, s0
	v_lshl_add_u64 v[12:13], v[12:13], 0, s[70:71]
	global_store_short v[12:13], v14, off
	v_mov_b32_e32 v100, v184
	v_mov_b32_e32 v101, v185
	s_nop 1
	v_mfma_f32_16x16x32_bf16 v[12:15], v[98:101], v[16:19], v[20:23]
